# FFN-up GEMM k-loop: reload the next phase's A fragments in place during the second MFMA block (moved out of the load segment), counted vmcnt before the post-MMA barriers
# baseline (speedup 1.0000x reference)
.LBB0_1649:
	ds_read_b128 v[130:133], v167
	ds_read_b128 v[134:137], v167 offset:1024
	ds_read_b128 v[138:141], v167 offset:2048
	ds_read_b128 v[142:145], v167 offset:3072
	ds_read_b128 v[168:171], v228
	ds_read_b128 v[172:175], v228 offset:1024
	ds_read_b128 v[176:179], v228 offset:2048
	ds_read_b128 v[180:183], v228 offset:3072
	s_add_u32 s38, s34, 0xfff80080
	s_addc_u32 s39, s35, -1
	s_cmp_eq_u32 s77, 28
	s_cselect_b32 s45, s1, s39
	s_cselect_b32 s44, s29, s38
	s_cselect_b32 s43, s27, s47
	s_cselect_b32 s42, s41, s46
	v_lshl_add_u64 v[146:147], s[34:35], 0, v[158:159]
	s_add_i32 m0, s50, 0xc000
	s_cmp_lg_u32 s77, -2
	s_cbranch_scc1 .Lga_P8_skipA
	ds_read_b128 v[184:187], v229
	ds_read_b128 v[188:191], v229 offset:1024
	ds_read_b128 v[192:195], v229 offset:2048
	ds_read_b128 v[196:199], v229 offset:3072
	ds_read_b128 v[200:203], v229 offset:4096
	ds_read_b128 v[204:207], v229 offset:5120
	ds_read_b128 v[208:211], v229 offset:6144
	ds_read_b128 v[212:215], v229 offset:7168
.Lga_P8_skipA:
	global_load_lds_dwordx4 v[146:147], off
	v_lshl_add_u64 v[146:147], s[34:35], 0, v[160:161]
	s_add_i32 m0, s50, 0xe000
	s_nop 0
	global_load_lds_dwordx4 v[146:147], off
	s_waitcnt vmcnt(8)
	s_waitcnt lgkmcnt(0)
	s_barrier
	s_setprio 1
	s_waitcnt lgkmcnt(0)
	v_mfma_i32_16x16x64_i8 v[46:49], v[130:133], v[184:187], v[46:49]
	v_mfma_i32_16x16x64_i8 v[34:37], v[138:141], v[184:187], v[34:37]
	v_mfma_i32_16x16x64_i8 v[42:45], v[130:133], v[192:195], v[42:45]
	v_mfma_i32_16x16x64_i8 v[30:33], v[138:141], v[192:195], v[30:33]
	v_mfma_i32_16x16x64_i8 v[38:41], v[130:133], v[200:203], v[38:41]
	v_mfma_i32_16x16x64_i8 v[26:29], v[138:141], v[200:203], v[26:29]
	v_mfma_i32_16x16x64_i8 v[126:129], v[130:133], v[208:211], v[126:129]
	v_mfma_i32_16x16x64_i8 v[122:125], v[138:141], v[208:211], v[122:125]
	v_mfma_i32_16x16x64_i8 v[46:49], v[134:137], v[188:191], v[46:49]
	v_mfma_i32_16x16x64_i8 v[34:37], v[142:145], v[188:191], v[34:37]
	v_mfma_i32_16x16x64_i8 v[42:45], v[134:137], v[196:199], v[42:45]
	v_mfma_i32_16x16x64_i8 v[30:33], v[142:145], v[196:199], v[30:33]
	v_mfma_i32_16x16x64_i8 v[38:41], v[134:137], v[204:207], v[38:41]
	v_mfma_i32_16x16x64_i8 v[26:29], v[142:145], v[204:207], v[26:29]
	v_mfma_i32_16x16x64_i8 v[126:129], v[134:137], v[212:215], v[126:129]
	v_mfma_i32_16x16x64_i8 v[122:125], v[142:145], v[212:215], v[122:125]
	s_setprio 0
	s_setprio 1
	v_mfma_i32_16x16x64_i8 v[22:25], v[168:171], v[184:187], v[22:25]
	v_mfma_i32_16x16x64_i8 v[10:13], v[176:179], v[184:187], v[10:13]
	ds_read_b128 v[184:187], v229 offset:16384
	v_mfma_i32_16x16x64_i8 v[18:21], v[168:171], v[192:195], v[18:21]
	v_mfma_i32_16x16x64_i8 v[6:9], v[176:179], v[192:195], v[6:9]
	ds_read_b128 v[192:195], v229 offset:18432
	v_mfma_i32_16x16x64_i8 v[14:17], v[168:171], v[200:203], v[14:17]
	v_mfma_i32_16x16x64_i8 v[2:5], v[176:179], v[200:203], v[2:5]
	ds_read_b128 v[200:203], v229 offset:20480
	v_mfma_i32_16x16x64_i8 v[118:121], v[168:171], v[208:211], v[118:121]
	v_mfma_i32_16x16x64_i8 v[114:117], v[176:179], v[208:211], v[114:117]
	ds_read_b128 v[208:211], v229 offset:22528
	v_mfma_i32_16x16x64_i8 v[22:25], v[172:175], v[188:191], v[22:25]
	v_mfma_i32_16x16x64_i8 v[10:13], v[180:183], v[188:191], v[10:13]
	ds_read_b128 v[188:191], v229 offset:17408
	v_mfma_i32_16x16x64_i8 v[18:21], v[172:175], v[196:199], v[18:21]
	v_mfma_i32_16x16x64_i8 v[6:9], v[180:183], v[196:199], v[6:9]
	ds_read_b128 v[196:199], v229 offset:19456
	v_mfma_i32_16x16x64_i8 v[14:17], v[172:175], v[204:207], v[14:17]
	v_mfma_i32_16x16x64_i8 v[2:5], v[180:183], v[204:207], v[2:5]
	ds_read_b128 v[204:207], v229 offset:21504
	v_mfma_i32_16x16x64_i8 v[118:121], v[172:175], v[212:215], v[118:121]
	v_mfma_i32_16x16x64_i8 v[114:117], v[180:183], v[212:215], v[114:117]
	ds_read_b128 v[212:215], v229 offset:23552
	s_setprio 0
	s_waitcnt vmcnt(2)
	s_barrier
	s_add_i32 s38, s64, s49
	v_lshl_add_u64 v[146:147], s[42:43], 0, v[150:151]
	s_mov_b32 m0, s38
	s_nop 0
	global_load_lds_dwordx4 v[146:147], off
	s_add_i32 m0, s38, 0x2000
	s_add_u32 s38, s42, 0x80000
	v_lshl_add_u64 v[216:217], s[42:43], 0, v[154:155]
	s_addc_u32 s39, s43, 0
	s_add_i32 s78, s65, s49
	global_load_lds_dwordx4 v[216:217], off
	v_lshl_add_u64 v[218:219], s[38:39], 0, v[150:151]
	s_mov_b32 m0, s78
	v_lshl_add_u64 v[220:221], s[44:45], 0, v[152:153]
	global_load_lds_dwordx4 v[218:219], off
	v_lshl_add_u64 v[218:219], s[38:39], 0, v[154:155]
	s_add_i32 m0, s78, 0x2000
	s_nop 0
	global_load_lds_dwordx4 v[218:219], off
	v_lshl_add_u64 v[218:219], s[44:45], 0, v[148:149]
	s_mov_b32 m0, s50
	s_nop 0
	global_load_lds_dwordx4 v[218:219], off
	s_mov_b32 m0, s51
	s_nop 0
	global_load_lds_dwordx4 v[220:221], off
	s_waitcnt vmcnt(8)
	s_waitcnt lgkmcnt(0)
	s_barrier
	s_setprio 1
	s_waitcnt lgkmcnt(0)
	v_mfma_i32_16x16x64_i8 v[94:97], v[130:133], v[184:187], v[94:97]
	v_mfma_i32_16x16x64_i8 v[70:73], v[138:141], v[184:187], v[70:73]
	v_mfma_i32_16x16x64_i8 v[86:89], v[130:133], v[192:195], v[86:89]
	v_mfma_i32_16x16x64_i8 v[62:65], v[138:141], v[192:195], v[62:65]
	v_mfma_i32_16x16x64_i8 v[78:81], v[130:133], v[200:203], v[78:81]
	v_mfma_i32_16x16x64_i8 v[54:57], v[138:141], v[200:203], v[54:57]
	v_mfma_i32_16x16x64_i8 v[110:113], v[130:133], v[208:211], v[110:113]
	v_mfma_i32_16x16x64_i8 v[106:109], v[138:141], v[208:211], v[106:109]
	v_mfma_i32_16x16x64_i8 v[94:97], v[134:137], v[188:191], v[94:97]
	v_mfma_i32_16x16x64_i8 v[70:73], v[142:145], v[188:191], v[70:73]
	v_mfma_i32_16x16x64_i8 v[86:89], v[134:137], v[196:199], v[86:89]
	v_mfma_i32_16x16x64_i8 v[62:65], v[142:145], v[196:199], v[62:65]
	v_mfma_i32_16x16x64_i8 v[78:81], v[134:137], v[204:207], v[78:81]
	v_mfma_i32_16x16x64_i8 v[54:57], v[142:145], v[204:207], v[54:57]
	v_mfma_i32_16x16x64_i8 v[110:113], v[134:137], v[212:215], v[110:113]
	v_mfma_i32_16x16x64_i8 v[106:109], v[142:145], v[212:215], v[106:109]
	s_setprio 0
	s_setprio 1
	v_mfma_i32_16x16x64_i8 v[90:93], v[168:171], v[184:187], v[90:93]
	v_mfma_i32_16x16x64_i8 v[66:69], v[176:179], v[184:187], v[66:69]
	ds_read_b128 v[184:187], v229 offset:32768
	v_mfma_i32_16x16x64_i8 v[82:85], v[168:171], v[192:195], v[82:85]
	v_mfma_i32_16x16x64_i8 v[58:61], v[176:179], v[192:195], v[58:61]
	ds_read_b128 v[192:195], v229 offset:34816
	v_mfma_i32_16x16x64_i8 v[74:77], v[168:171], v[200:203], v[74:77]
	v_mfma_i32_16x16x64_i8 v[50:53], v[176:179], v[200:203], v[50:53]
	ds_read_b128 v[200:203], v229 offset:36864
	v_mfma_i32_16x16x64_i8 v[102:105], v[168:171], v[208:211], v[102:105]
	v_mfma_i32_16x16x64_i8 v[98:101], v[176:179], v[208:211], v[98:101]
	ds_read_b128 v[208:211], v229 offset:38912
	v_mfma_i32_16x16x64_i8 v[90:93], v[172:175], v[188:191], v[90:93]
	v_mfma_i32_16x16x64_i8 v[66:69], v[180:183], v[188:191], v[66:69]
	ds_read_b128 v[188:191], v229 offset:33792
	v_mfma_i32_16x16x64_i8 v[82:85], v[172:175], v[196:199], v[82:85]
	v_mfma_i32_16x16x64_i8 v[58:61], v[180:183], v[196:199], v[58:61]
	ds_read_b128 v[196:199], v229 offset:35840
	v_mfma_i32_16x16x64_i8 v[74:77], v[172:175], v[204:207], v[74:77]
	v_mfma_i32_16x16x64_i8 v[50:53], v[180:183], v[204:207], v[50:53]
	ds_read_b128 v[204:207], v229 offset:37888
	v_mfma_i32_16x16x64_i8 v[102:105], v[172:175], v[212:215], v[102:105]
	v_mfma_i32_16x16x64_i8 v[98:101], v[180:183], v[212:215], v[98:101]
	ds_read_b128 v[212:215], v229 offset:39936
	s_setprio 0
	s_waitcnt vmcnt(6)
	s_barrier
	s_add_i32 s78, 0, 0x18000
	s_add_i32 s79, 0, 0x1c000
	v_add_u32_e32 v142, s78, v1
	v_add_u32_e32 v156, s79, v1
	ds_read_b128 v[130:133], v142
	ds_read_b128 v[134:137], v142 offset:1024
	ds_read_b128 v[138:141], v142 offset:2048
	ds_read_b128 v[142:145], v142 offset:3072
	ds_read_b128 v[168:171], v156
	ds_read_b128 v[172:175], v156 offset:1024
	ds_read_b128 v[176:179], v156 offset:2048
	ds_read_b128 v[180:183], v156 offset:3072
	s_add_u32 s38, s44, 0x80000
	s_addc_u32 s39, s45, 0
	s_mov_b32 m0, s52
	v_lshl_add_u64 v[222:223], s[38:39], 0, v[148:149]
	global_load_lds_dwordx4 v[222:223], off
	v_lshl_add_u64 v[222:223], s[38:39], 0, v[152:153]
	s_mov_b32 m0, s53
	s_nop 0
	global_load_lds_dwordx4 v[222:223], off
	s_waitcnt vmcnt(8)
	s_waitcnt lgkmcnt(0)
	s_barrier
	s_setprio 1
	s_waitcnt lgkmcnt(0)
	v_mfma_i32_16x16x64_i8 v[46:49], v[130:133], v[184:187], v[46:49]
	v_mfma_i32_16x16x64_i8 v[34:37], v[138:141], v[184:187], v[34:37]
	v_mfma_i32_16x16x64_i8 v[42:45], v[130:133], v[192:195], v[42:45]
	v_mfma_i32_16x16x64_i8 v[30:33], v[138:141], v[192:195], v[30:33]
	v_mfma_i32_16x16x64_i8 v[38:41], v[130:133], v[200:203], v[38:41]
	v_mfma_i32_16x16x64_i8 v[26:29], v[138:141], v[200:203], v[26:29]
	v_mfma_i32_16x16x64_i8 v[126:129], v[130:133], v[208:211], v[126:129]
	v_mfma_i32_16x16x64_i8 v[122:125], v[138:141], v[208:211], v[122:125]
	v_mfma_i32_16x16x64_i8 v[46:49], v[134:137], v[188:191], v[46:49]
	v_mfma_i32_16x16x64_i8 v[34:37], v[142:145], v[188:191], v[34:37]
	v_mfma_i32_16x16x64_i8 v[42:45], v[134:137], v[196:199], v[42:45]
	v_mfma_i32_16x16x64_i8 v[30:33], v[142:145], v[196:199], v[30:33]
	v_mfma_i32_16x16x64_i8 v[38:41], v[134:137], v[204:207], v[38:41]
	v_mfma_i32_16x16x64_i8 v[26:29], v[142:145], v[204:207], v[26:29]
	v_mfma_i32_16x16x64_i8 v[126:129], v[134:137], v[212:215], v[126:129]
	v_mfma_i32_16x16x64_i8 v[122:125], v[142:145], v[212:215], v[122:125]
	s_setprio 0
	s_setprio 1
	v_mfma_i32_16x16x64_i8 v[22:25], v[168:171], v[184:187], v[22:25]
	v_mfma_i32_16x16x64_i8 v[10:13], v[176:179], v[184:187], v[10:13]
	ds_read_b128 v[184:187], v229 offset:49152
	v_mfma_i32_16x16x64_i8 v[18:21], v[168:171], v[192:195], v[18:21]
	v_mfma_i32_16x16x64_i8 v[6:9], v[176:179], v[192:195], v[6:9]
	ds_read_b128 v[192:195], v229 offset:51200
	v_mfma_i32_16x16x64_i8 v[14:17], v[168:171], v[200:203], v[14:17]
	v_mfma_i32_16x16x64_i8 v[2:5], v[176:179], v[200:203], v[2:5]
	ds_read_b128 v[200:203], v229 offset:53248
	v_mfma_i32_16x16x64_i8 v[118:121], v[168:171], v[208:211], v[118:121]
	v_mfma_i32_16x16x64_i8 v[114:117], v[176:179], v[208:211], v[114:117]
	ds_read_b128 v[208:211], v229 offset:55296
	v_mfma_i32_16x16x64_i8 v[22:25], v[172:175], v[188:191], v[22:25]
	v_mfma_i32_16x16x64_i8 v[10:13], v[180:183], v[188:191], v[10:13]
	ds_read_b128 v[188:191], v229 offset:50176
	v_mfma_i32_16x16x64_i8 v[18:21], v[172:175], v[196:199], v[18:21]
	v_mfma_i32_16x16x64_i8 v[6:9], v[180:183], v[196:199], v[6:9]
	ds_read_b128 v[196:199], v229 offset:52224
	v_mfma_i32_16x16x64_i8 v[14:17], v[172:175], v[204:207], v[14:17]
	v_mfma_i32_16x16x64_i8 v[2:5], v[180:183], v[204:207], v[2:5]
	ds_read_b128 v[204:207], v229 offset:54272
	v_mfma_i32_16x16x64_i8 v[118:121], v[172:175], v[212:215], v[118:121]
	v_mfma_i32_16x16x64_i8 v[114:117], v[180:183], v[212:215], v[114:117]
	ds_read_b128 v[212:215], v229 offset:56320
	s_setprio 0
	s_waitcnt vmcnt(2)
	s_barrier
	s_add_i32 s38, s78, s49
	v_lshl_add_u64 v[146:147], v[146:147], 0, s[14:15]
	s_mov_b32 m0, s38
	s_nop 0
	global_load_lds_dwordx4 v[146:147], off
	s_add_i32 m0, s38, 0x2000
	s_add_u32 s38, s42, 0x80080
	v_lshl_add_u64 v[146:147], v[216:217], 0, s[14:15]
	s_addc_u32 s39, s43, 0
	s_add_i32 s42, s79, s49
	global_load_lds_dwordx4 v[146:147], off
	v_lshl_add_u64 v[146:147], s[38:39], 0, v[150:151]
	s_mov_b32 m0, s42
	s_nop 0
	global_load_lds_dwordx4 v[146:147], off
	v_lshl_add_u64 v[146:147], s[38:39], 0, v[154:155]
	s_add_i32 m0, s42, 0x2000
	s_nop 0
	global_load_lds_dwordx4 v[146:147], off
	v_lshl_add_u64 v[146:147], v[218:219], 0, s[14:15]
	s_mov_b32 m0, s57
	s_nop 0
	global_load_lds_dwordx4 v[146:147], off
	v_lshl_add_u64 v[146:147], v[220:221], 0, s[14:15]
	s_mov_b32 m0, s58
	s_nop 0
	global_load_lds_dwordx4 v[146:147], off
	s_waitcnt vmcnt(8)
	s_waitcnt lgkmcnt(0)
	s_barrier
	s_setprio 1
	s_waitcnt lgkmcnt(0)
	v_mfma_i32_16x16x64_i8 v[94:97], v[130:133], v[184:187], v[94:97]
	v_mfma_i32_16x16x64_i8 v[70:73], v[138:141], v[184:187], v[70:73]
	v_mfma_i32_16x16x64_i8 v[86:89], v[130:133], v[192:195], v[86:89]
	v_mfma_i32_16x16x64_i8 v[62:65], v[138:141], v[192:195], v[62:65]
	v_mfma_i32_16x16x64_i8 v[78:81], v[130:133], v[200:203], v[78:81]
	v_mfma_i32_16x16x64_i8 v[54:57], v[138:141], v[200:203], v[54:57]
	v_mfma_i32_16x16x64_i8 v[110:113], v[130:133], v[208:211], v[110:113]
	v_mfma_i32_16x16x64_i8 v[106:109], v[138:141], v[208:211], v[106:109]
	v_mfma_i32_16x16x64_i8 v[94:97], v[134:137], v[188:191], v[94:97]
	v_mfma_i32_16x16x64_i8 v[70:73], v[142:145], v[188:191], v[70:73]
	v_mfma_i32_16x16x64_i8 v[86:89], v[134:137], v[196:199], v[86:89]
	v_mfma_i32_16x16x64_i8 v[62:65], v[142:145], v[196:199], v[62:65]
	v_mfma_i32_16x16x64_i8 v[78:81], v[134:137], v[204:207], v[78:81]
	v_mfma_i32_16x16x64_i8 v[54:57], v[142:145], v[204:207], v[54:57]
	v_mfma_i32_16x16x64_i8 v[110:113], v[134:137], v[212:215], v[110:113]
	v_mfma_i32_16x16x64_i8 v[106:109], v[142:145], v[212:215], v[106:109]
	s_setprio 0
	s_setprio 1
	v_mfma_i32_16x16x64_i8 v[90:93], v[168:171], v[184:187], v[90:93]
	v_mfma_i32_16x16x64_i8 v[66:69], v[176:179], v[184:187], v[66:69]
	ds_read_b128 v[184:187], v229
	v_mfma_i32_16x16x64_i8 v[82:85], v[168:171], v[192:195], v[82:85]
	v_mfma_i32_16x16x64_i8 v[58:61], v[176:179], v[192:195], v[58:61]
	ds_read_b128 v[192:195], v229 offset:2048
	v_mfma_i32_16x16x64_i8 v[74:77], v[168:171], v[200:203], v[74:77]
	v_mfma_i32_16x16x64_i8 v[50:53], v[176:179], v[200:203], v[50:53]
	ds_read_b128 v[200:203], v229 offset:4096
	v_mfma_i32_16x16x64_i8 v[102:105], v[168:171], v[208:211], v[102:105]
	v_mfma_i32_16x16x64_i8 v[98:101], v[176:179], v[208:211], v[98:101]
	ds_read_b128 v[208:211], v229 offset:6144
	v_mfma_i32_16x16x64_i8 v[90:93], v[172:175], v[188:191], v[90:93]
	v_mfma_i32_16x16x64_i8 v[66:69], v[180:183], v[188:191], v[66:69]
	ds_read_b128 v[188:191], v229 offset:1024
	v_mfma_i32_16x16x64_i8 v[82:85], v[172:175], v[196:199], v[82:85]
	v_mfma_i32_16x16x64_i8 v[58:61], v[180:183], v[196:199], v[58:61]
	ds_read_b128 v[196:199], v229 offset:3072
	v_mfma_i32_16x16x64_i8 v[74:77], v[172:175], v[204:207], v[74:77]
	v_mfma_i32_16x16x64_i8 v[50:53], v[180:183], v[204:207], v[50:53]
	ds_read_b128 v[204:207], v229 offset:5120
	v_mfma_i32_16x16x64_i8 v[102:105], v[172:175], v[212:215], v[102:105]
	v_mfma_i32_16x16x64_i8 v[98:101], v[180:183], v[212:215], v[98:101]
	ds_read_b128 v[212:215], v229 offset:7168
	s_setprio 0
	s_waitcnt vmcnt(6)
	s_barrier
	s_add_i32 s77, s77, 2
	s_add_u32 s34, s34, 0x100
	s_addc_u32 s35, s35, 0
	s_add_u32 s46, s46, 0x100
	s_addc_u32 s47, s47, 0
	s_cmp_gt_u32 s77, 29
	s_cbranch_scc0 .LBB0_1649
	s_waitcnt lgkmcnt(0)
	s_and_b64 vcc, exec, s[16:17]
	s_cbranch_vccz .LBB0_1652
	s_barrier
